# in-proj rope epilogue: the 7 later rope-table lines touched up front; on top of v33
# baseline (speedup 1.0000x reference)
;     __device__ __forceinline__ void operator()(const f32x4 (&acc)[2][2][4][2], const Unit& u, int wr, int wc, int fr, int fq) const {
;     ...
;                 for (int m = 0; m < 4; ++m) { const int row = row0 + ai * HALF + m * 16;
;                     f32x4 cs0 = (f32x4){1.f, 1.f, 1.f, 1.f}, cs1 = cs0, sn0 = (f32x4){0.f, 0.f, 0.f, 0.f}, sn1 = sn0;
;                     if (wc == 0) { const float* rp = rope + (size_t)row * 32 + 8 * (fq & 1); cs0 = *(const f32x4*)rp; cs1 = *(const f32x4*)(rp + 4); sn0 = *(const f32x4*)(rp + 16) * sgn; sn1 = *(const f32x4*)(rp + 20) * sgn; }
.LBB0_258:
	v_lshlrev_b64 v[128:129], 7, v[160:161]
	v_lshl_add_u64 v[132:133], v[152:153], 0, v[128:129]
	global_load_dword v184, v[132:133], off offset:2048
	v_add_co_u32_e32 v186, vcc, 0x1000, v132
	s_nop 1
	v_addc_co_u32_e32 v187, vcc, 0, v133, vcc
	global_load_dword v184, v[186:187], off
	global_load_dword v184, v[186:187], off offset:2048
	v_add_co_u32_e32 v186, vcc, 0x4000, v132
	s_nop 1
	v_addc_co_u32_e32 v187, vcc, 0, v133, vcc
	global_load_dword v184, v[186:187], off
	global_load_dword v184, v[186:187], off offset:2048
	v_add_co_u32_e32 v186, vcc, 0x5000, v132
	s_nop 1
	v_addc_co_u32_e32 v187, vcc, 0, v133, vcc
	global_load_dword v184, v[186:187], off
	global_load_dword v184, v[186:187], off offset:2048
	global_load_dwordx4 v[162:165], v[132:133], off offset:64
	global_load_dwordx4 v[180:183], v[132:133], off offset:80
	global_load_dwordx4 v[128:131], v[132:133], off offset:16
	s_nop 0
	global_load_dwordx4 v[132:135], v[132:133], off
	s_waitcnt vmcnt(0)
	v_pk_mul_f32 v[168:169], v[148:149], v[164:165]
	v_pk_mul_f32 v[170:171], v[146:147], v[162:163]
	v_pk_mul_f32 v[164:165], v[148:149], v[182:183]
	v_pk_mul_f32 v[166:167], v[146:147], v[180:181]
	s_and_b64 vcc, exec, s[2:3]
	s_cbranch_vccnz .LBB0_211
	s_branch .LBB0_210
